# stick-breaking unmasked tile arm rewritten as plain scalar f32 ops (keep=rcp(1+e), running products, weights): same operations, the compiler's 42 register shuffles and 25 packed ops per tile removed
# baseline (speedup 1.0000x reference)
;     ...
;                     if (diag) { asm volatile("; stick-breaking: diagonal tile (masked)" ::: "memory"); SB_GROUPS(true) } else { SB_GROUPS(false) }
.LBB0_428:
	s_andn2_b64 vcc, exec, s[20:21]
	s_cbranch_vccnz .LBB0_430
	v_add_f32_e32 v25, 1.0, v93
	v_rcp_f32_e32 v25, v25
	v_add_f32_e32 v24, 1.0, v92
	v_rcp_f32_e32 v24, v24
	v_add_f32_e32 v27, 1.0, v91
	v_rcp_f32_e32 v27, v27
	v_add_f32_e32 v26, 1.0, v90
	v_rcp_f32_e32 v26, v26
	v_add_f32_e32 v19, 1.0, v97
	v_rcp_f32_e32 v19, v19
	v_add_f32_e32 v18, 1.0, v95
	v_rcp_f32_e32 v18, v18
	v_add_f32_e32 v23, 1.0, v96
	v_rcp_f32_e32 v23, v23
	v_add_f32_e32 v22, 1.0, v94
	v_rcp_f32_e32 v22, v22
	v_mul_f32_e32 v20, v25, v24
	v_sub_f32_e32 v24, v25, v20
	v_mul_f32_e32 v200, v27, v20
	v_sub_f32_e32 v25, v201, v25
	v_sub_f32_e32 v27, v20, v200
	v_mul_f32_e32 v20, v26, v200
	v_sub_f32_e32 v26, v200, v20
	v_add_f32_e32 v39, 1.0, v79
	v_rcp_f32_e32 v39, v39
	v_add_f32_e32 v38, 1.0, v78
	v_rcp_f32_e32 v38, v38
	v_add_f32_e32 v37, 1.0, v77
	v_rcp_f32_e32 v37, v37
	v_add_f32_e32 v36, 1.0, v76
	v_rcp_f32_e32 v36, v36
	v_mul_f32_e32 v21, v19, v18
	v_sub_f32_e32 v18, v19, v21
	v_mul_f32_e32 v45, v23, v21
	v_sub_f32_e32 v19, v201, v19
	v_sub_f32_e32 v23, v21, v45
	v_mul_f32_e32 v21, v22, v45
	v_sub_f32_e32 v22, v45, v21
	v_add_f32_e32 v29, 1.0, v82
	v_rcp_f32_e32 v29, v29
	v_add_f32_e32 v28, 1.0, v83
	v_rcp_f32_e32 v28, v28
	v_add_f32_e32 v31, 1.0, v81
	v_rcp_f32_e32 v31, v31
	v_add_f32_e32 v30, 1.0, v80
	v_rcp_f32_e32 v30, v30
	v_mul_f32_e32 v32, v39, v38
	v_sub_f32_e32 v38, v39, v32
	v_mul_f32_e32 v200, v37, v32
	v_sub_f32_e32 v39, v201, v39
	v_sub_f32_e32 v37, v32, v200
	v_mul_f32_e32 v32, v36, v200
	v_sub_f32_e32 v36, v200, v32
	v_add_f32_e32 v41, 1.0, v75
	v_rcp_f32_e32 v41, v41
	v_add_f32_e32 v40, 1.0, v74
	v_rcp_f32_e32 v40, v40
	v_add_f32_e32 v43, 1.0, v73
	v_rcp_f32_e32 v43, v43
	v_add_f32_e32 v42, 1.0, v72
	v_rcp_f32_e32 v42, v42
	v_mul_f32_e32 v33, v29, v28
	v_sub_f32_e32 v28, v29, v33
	v_mul_f32_e32 v45, v31, v33
	v_sub_f32_e32 v29, v201, v29
	v_sub_f32_e32 v31, v33, v45
	v_mul_f32_e32 v33, v30, v45
	v_sub_f32_e32 v30, v45, v33
	v_add_f32_e32 v47, 1.0, v71
	v_rcp_f32_e32 v47, v47
	v_add_f32_e32 v46, 1.0, v70
	v_rcp_f32_e32 v46, v46
	v_add_f32_e32 v49, 1.0, v69
	v_rcp_f32_e32 v49, v49
	v_add_f32_e32 v48, 1.0, v68
	v_rcp_f32_e32 v48, v48
	v_mul_f32_e32 v44, v41, v40
	v_sub_f32_e32 v40, v41, v44
	v_mul_f32_e32 v200, v43, v44
	v_sub_f32_e32 v41, v201, v41
	v_sub_f32_e32 v43, v44, v200
	v_mul_f32_e32 v44, v42, v200
	v_sub_f32_e32 v42, v200, v44
	v_add_f32_e32 v61, 1.0, v63
	v_rcp_f32_e32 v61, v61
	v_add_f32_e32 v60, 1.0, v62
	v_rcp_f32_e32 v60, v60
	v_add_f32_e32 v59, 1.0, v34
	v_rcp_f32_e32 v59, v59
	v_add_f32_e32 v58, 1.0, v1
	v_rcp_f32_e32 v58, v58
	v_mul_f32_e32 v50, v47, v46
	v_sub_f32_e32 v46, v47, v50
	v_mul_f32_e32 v45, v49, v50
	v_sub_f32_e32 v47, v201, v47
	v_sub_f32_e32 v49, v50, v45
	v_mul_f32_e32 v50, v48, v45
	v_sub_f32_e32 v48, v45, v50
	v_add_f32_e32 v53, 1.0, v67
	v_rcp_f32_e32 v53, v53
	v_add_f32_e32 v52, 1.0, v66
	v_rcp_f32_e32 v52, v52
	v_add_f32_e32 v55, 1.0, v65
	v_rcp_f32_e32 v55, v55
	v_add_f32_e32 v54, 1.0, v64
	v_rcp_f32_e32 v54, v54
	v_mul_f32_e32 v56, v61, v60
	v_sub_f32_e32 v60, v61, v56
	v_mul_f32_e32 v200, v59, v56
	v_sub_f32_e32 v61, v201, v61
	v_sub_f32_e32 v59, v56, v200
	v_mul_f32_e32 v56, v58, v200
	v_sub_f32_e32 v58, v200, v56
	s_nop 0
	v_mul_f32_e32 v57, v53, v52
	v_sub_f32_e32 v52, v53, v57
	v_mul_f32_e32 v45, v55, v57
	v_sub_f32_e32 v53, v201, v53
	v_sub_f32_e32 v55, v57, v45
	v_mul_f32_e32 v57, v54, v45
	v_sub_f32_e32 v54, v45, v57

;     ...
;                     if (diag) { asm volatile("; stick-breaking: diagonal tile (masked)" ::: "memory"); SB_GROUPS(true) } else { SB_GROUPS(false) }
.LBB0_476:
	s_andn2_b64 vcc, exec, s[30:31]
	s_cbranch_vccnz .LBB0_478
	v_add_f32_e32 v59, 1.0, v151
	v_rcp_f32_e32 v59, v59
	v_add_f32_e32 v58, 1.0, v150
	v_rcp_f32_e32 v58, v58
	v_add_f32_e32 v61, 1.0, v149
	v_rcp_f32_e32 v61, v61
	v_add_f32_e32 v60, 1.0, v131
	v_rcp_f32_e32 v60, v60
	v_add_f32_e32 v53, 1.0, v155
	v_rcp_f32_e32 v53, v53
	v_add_f32_e32 v52, 1.0, v153
	v_rcp_f32_e32 v52, v52
	v_add_f32_e32 v57, 1.0, v154
	v_rcp_f32_e32 v57, v57
	v_add_f32_e32 v56, 1.0, v152
	v_rcp_f32_e32 v56, v56
	v_mul_f32_e32 v54, v59, v58
	v_sub_f32_e32 v58, v59, v54
	v_mul_f32_e32 v200, v61, v54
	v_sub_f32_e32 v59, v201, v59
	v_sub_f32_e32 v61, v54, v200
	v_mul_f32_e32 v54, v60, v200
	v_sub_f32_e32 v60, v200, v54
	v_add_f32_e32 v71, 1.0, v126
	v_rcp_f32_e32 v71, v71
	v_add_f32_e32 v70, 1.0, v125
	v_rcp_f32_e32 v70, v70
	v_add_f32_e32 v69, 1.0, v124
	v_rcp_f32_e32 v69, v69
	v_add_f32_e32 v68, 1.0, v123
	v_rcp_f32_e32 v68, v68
	v_mul_f32_e32 v55, v53, v52
	v_sub_f32_e32 v52, v53, v55
	v_mul_f32_e32 v77, v57, v55
	v_sub_f32_e32 v53, v201, v53
	v_sub_f32_e32 v57, v55, v77
	v_mul_f32_e32 v55, v56, v77
	v_sub_f32_e32 v56, v77, v55
	v_add_f32_e32 v63, 1.0, v129
	v_rcp_f32_e32 v63, v63
	v_add_f32_e32 v62, 1.0, v130
	v_rcp_f32_e32 v62, v62
	v_add_f32_e32 v65, 1.0, v128
	v_rcp_f32_e32 v65, v65
	v_add_f32_e32 v64, 1.0, v127
	v_rcp_f32_e32 v64, v64
	v_mul_f32_e32 v66, v71, v70
	v_sub_f32_e32 v70, v71, v66
	v_mul_f32_e32 v200, v69, v66
	v_sub_f32_e32 v71, v201, v71
	v_sub_f32_e32 v69, v66, v200
	v_mul_f32_e32 v66, v68, v200
	v_sub_f32_e32 v68, v200, v66
	v_add_f32_e32 v73, 1.0, v122
	v_rcp_f32_e32 v73, v73
	v_add_f32_e32 v72, 1.0, v121
	v_rcp_f32_e32 v72, v72
	v_add_f32_e32 v75, 1.0, v120
	v_rcp_f32_e32 v75, v75
	v_add_f32_e32 v74, 1.0, v119
	v_rcp_f32_e32 v74, v74
	v_mul_f32_e32 v67, v63, v62
	v_sub_f32_e32 v62, v63, v67
	v_mul_f32_e32 v77, v65, v67
	v_sub_f32_e32 v63, v201, v63
	v_sub_f32_e32 v65, v67, v77
	v_mul_f32_e32 v67, v64, v77
	v_sub_f32_e32 v64, v77, v67
	v_add_f32_e32 v79, 1.0, v118
	v_rcp_f32_e32 v79, v79
	v_add_f32_e32 v78, 1.0, v117
	v_rcp_f32_e32 v78, v78
	v_add_f32_e32 v81, 1.0, v115
	v_rcp_f32_e32 v81, v81
	v_add_f32_e32 v80, 1.0, v114
	v_rcp_f32_e32 v80, v80
	v_mul_f32_e32 v76, v73, v72
	v_sub_f32_e32 v72, v73, v76
	v_mul_f32_e32 v200, v75, v76
	v_sub_f32_e32 v73, v201, v73
	v_sub_f32_e32 v75, v76, v200
	v_mul_f32_e32 v76, v74, v200
	v_sub_f32_e32 v74, v200, v76
	v_add_f32_e32 v101, 1.0, v109
	v_rcp_f32_e32 v101, v101
	v_add_f32_e32 v100, 1.0, v108
	v_rcp_f32_e32 v100, v100
	v_add_f32_e32 v99, 1.0, v91
	v_rcp_f32_e32 v99, v99
	v_add_f32_e32 v98, 1.0, v34
	v_rcp_f32_e32 v98, v98
	v_mul_f32_e32 v82, v79, v78
	v_sub_f32_e32 v78, v79, v82
	v_mul_f32_e32 v77, v81, v82
	v_sub_f32_e32 v79, v201, v79
	v_sub_f32_e32 v81, v82, v77
	v_mul_f32_e32 v82, v80, v77
	v_sub_f32_e32 v80, v77, v82
	v_add_f32_e32 v93, 1.0, v113
	v_rcp_f32_e32 v93, v93
	v_add_f32_e32 v92, 1.0, v112
	v_rcp_f32_e32 v92, v92
	v_add_f32_e32 v95, 1.0, v111
	v_rcp_f32_e32 v95, v95
	v_add_f32_e32 v94, 1.0, v110
	v_rcp_f32_e32 v94, v94
	v_mul_f32_e32 v96, v101, v100
	v_sub_f32_e32 v100, v101, v96
	v_mul_f32_e32 v200, v99, v96
	v_sub_f32_e32 v101, v201, v101
	v_sub_f32_e32 v99, v96, v200
	v_mul_f32_e32 v96, v98, v200
	v_sub_f32_e32 v98, v200, v96
	s_nop 0
	v_mul_f32_e32 v97, v93, v92
	v_sub_f32_e32 v92, v93, v97
	v_mul_f32_e32 v77, v95, v97
	v_sub_f32_e32 v93, v201, v93
	v_sub_f32_e32 v95, v97, v77
	v_mul_f32_e32 v97, v94, v77
	v_sub_f32_e32 v94, v77, v97
